# attn_fast: first barrier waits only for q,k (vmcnt 11); key-state/gate/prefix tiles get a second counted wait + barrier right before N1 (both wave halves)
# baseline (speedup 1.0000x reference)
.LBB12_14:
	s_or_b64 exec, exec, s[0:1]
	v_lshrrev_b32_e32 v105, 2, v0
	v_and_b32_e32 v103, 15, v0
	v_lshrrev_b32_e32 v2, 4, v0
	v_bfe_u32 v104, v0, 4, 2
	v_and_or_b32 v102, v105, 48, v103
	s_add_i32 s33, 0, 0x18000
	v_bitop3_b32 v2, v2, v103, 3 bitop3:0x6c
	v_lshl_add_u32 v3, v102, 9, s33
	v_lshlrev_b32_e32 v78, 4, v2
	v_bitop3_b32 v4, v104, v103, 4 bitop3:0x36
	v_add_u32_e32 v2, v3, v78
	v_lshlrev_b32_e32 v77, 4, v4
	s_waitcnt vmcnt(11)
	s_barrier
	v_add_u32_e32 v4, v3, v77
	ds_read_b128 v[62:65], v2
	ds_read_b128 v[58:61], v4
	v_bitop3_b32 v2, v104, v103, 8 bitop3:0x36
	v_lshlrev_b32_e32 v76, 4, v2
	v_bitop3_b32 v4, v104, v103, 12 bitop3:0x36
	v_add_u32_e32 v2, v3, v76
	v_lshlrev_b32_e32 v75, 4, v4
	v_add_u32_e32 v4, v3, v75
	ds_read_b128 v[54:57], v2
	ds_read_b128 v[50:53], v4
	v_bitop3_b32 v2, v104, v103, 16 bitop3:0x36
	v_lshlrev_b32_e32 v74, 4, v2
	v_bitop3_b32 v4, v104, v103, 20 bitop3:0x36
	v_add_u32_e32 v2, v3, v74
	v_lshlrev_b32_e32 v72, 4, v4
	v_add_u32_e32 v4, v3, v72
	ds_read_b128 v[46:49], v2
	ds_read_b128 v[42:45], v4
	v_bitop3_b32 v2, v104, v103, 24 bitop3:0x36
	v_lshlrev_b32_e32 v73, 4, v2
	v_bitop3_b32 v4, v104, v103, 28 bitop3:0x36
	v_add_u32_e32 v2, v3, v73
	v_lshlrev_b32_e32 v71, 4, v4
	v_add_u32_e32 v3, v3, v71
	ds_read_b128 v[38:41], v2
	ds_read_b128 v[34:37], v3
	s_waitcnt lgkmcnt(0)
	v_lshl_add_u64 v[66:67], s[36:37], 0, v[66:67]
	s_mov_b64 s[0:1], 0
	s_movk_i32 s6, 0x70
	s_mov_b64 s[4:5], 0x2000
	s_movk_i32 s7, 0x5ff
	v_mov_b32_e32 v69, 0
	s_barrier
.LBB12_15:
	v_add_u32_e32 v79, s33, v70
	v_bitop3_b32 v68, v70, s6, v1 bitop3:0x48
	v_readfirstlane_b32 s8, v79
	v_lshl_add_u64 v[80:81], v[66:67], 0, v[68:69]
	s_mov_b32 m0, s8
	v_add_u32_e32 v68, 0x200, v1
	global_load_lds_dwordx4 v[80:81], off
	v_cmp_lt_u32_e32 vcc, s7, v1
	v_add_u32_e32 v70, 0x2000, v70
	v_lshl_add_u64 v[66:67], v[66:67], 0, s[4:5]
	s_or_b64 s[0:1], vcc, s[0:1]
	v_mov_b32_e32 v1, v68
	s_andn2_b64 exec, exec, s[0:1]
	s_cbranch_execnz .LBB12_15
	s_or_b64 exec, exec, s[0:1]
	v_readfirstlane_b32 s44, v0
	s_nop 3
	s_cmp_lt_u32 s44, 0x100
	s_cbranch_scc0 .Lat_dh1
	v_lshl_add_u32 v1, v103, 9, 0
	v_add_u32_e32 v114, v1, v78
	v_add_u32_e32 v117, v1, v77
	v_add_u32_e32 v115, v1, v76
	v_add_u32_e32 v113, v1, v75
	v_add_u32_e32 v119, v1, v74
	v_add_u32_e32 v118, v1, v72
	v_add_u32_e32 v116, v1, v73
	v_add_u32_e32 v1, v1, v71
	s_mov_b32 s38, 0x5040100
	s_add_u32 s36, s30, s34
	s_addc_u32 s37, s31, s35
	s_add_i32 s30, 0, 0x20000
	v_lshlrev_b32_e32 v112, 7, v103
	s_add_i32 s34, 0, 0x22000
	ds_read_b128 v[156:159], v114
	ds_read_b128 v[160:163], v117
	ds_read_b128 v[164:167], v115
	ds_read_b128 v[168:171], v113
	ds_read_b128 v[172:175], v119
	ds_read_b128 v[176:179], v118
	ds_read_b128 v[180:183], v116
	ds_read_b128 v[184:187], v1
	ds_read_b128 v[188:191], v114 offset:8192
	ds_read_b128 v[192:195], v117 offset:8192
	ds_read_b128 v[196:199], v115 offset:8192
	ds_read_b128 v[200:203], v113 offset:8192
	ds_read_b128 v[204:207], v119 offset:8192
	ds_read_b128 v[208:211], v118 offset:8192
	ds_read_b128 v[212:215], v116 offset:8192
	ds_read_b128 v[216:219], v1 offset:8192
	s_waitcnt lgkmcnt(8)
	v_mfma_f32_16x16x32_bf16 v[66:69], v[156:159], v[62:65], 0
	v_mfma_f32_16x16x32_bf16 v[66:69], v[160:163], v[58:61], v[66:69]
	v_mfma_f32_16x16x32_bf16 v[66:69], v[164:167], v[54:57], v[66:69]
	v_mfma_f32_16x16x32_bf16 v[66:69], v[168:171], v[50:53], v[66:69]
	v_mfma_f32_16x16x32_bf16 v[66:69], v[172:175], v[46:49], v[66:69]
	v_mfma_f32_16x16x32_bf16 v[66:69], v[176:179], v[42:45], v[66:69]
	v_mfma_f32_16x16x32_bf16 v[66:69], v[180:183], v[38:41], v[66:69]
	v_mfma_f32_16x16x32_bf16 v[66:69], v[184:187], v[34:37], v[66:69]
	s_waitcnt lgkmcnt(0)
	v_mfma_f32_16x16x32_bf16 v[70:73], v[188:191], v[62:65], 0
	v_mfma_f32_16x16x32_bf16 v[70:73], v[192:195], v[58:61], v[70:73]
	v_mfma_f32_16x16x32_bf16 v[70:73], v[196:199], v[54:57], v[70:73]
	v_mfma_f32_16x16x32_bf16 v[70:73], v[200:203], v[50:53], v[70:73]
	v_mfma_f32_16x16x32_bf16 v[70:73], v[204:207], v[46:49], v[70:73]
	v_mfma_f32_16x16x32_bf16 v[70:73], v[208:211], v[42:45], v[70:73]
	v_mfma_f32_16x16x32_bf16 v[70:73], v[212:215], v[38:41], v[70:73]
	v_mfma_f32_16x16x32_bf16 v[70:73], v[216:219], v[34:37], v[70:73]
	ds_read_b128 v[156:159], v114 offset:16384
	ds_read_b128 v[160:163], v117 offset:16384
	ds_read_b128 v[164:167], v115 offset:16384
	ds_read_b128 v[168:171], v113 offset:16384
	ds_read_b128 v[172:175], v119 offset:16384
	ds_read_b128 v[176:179], v118 offset:16384
	ds_read_b128 v[180:183], v116 offset:16384
	ds_read_b128 v[184:187], v1 offset:16384
	ds_read_b128 v[188:191], v114 offset:24576
	ds_read_b128 v[192:195], v117 offset:24576
	ds_read_b128 v[196:199], v115 offset:24576
	ds_read_b128 v[200:203], v113 offset:24576
	ds_read_b128 v[204:207], v119 offset:24576
	ds_read_b128 v[208:211], v118 offset:24576
	ds_read_b128 v[212:215], v116 offset:24576
	ds_read_b128 v[216:219], v1 offset:24576
	s_waitcnt lgkmcnt(8)
	v_mfma_f32_16x16x32_bf16 v[74:77], v[156:159], v[62:65], 0
	v_mfma_f32_16x16x32_bf16 v[74:77], v[160:163], v[58:61], v[74:77]
	v_mfma_f32_16x16x32_bf16 v[74:77], v[164:167], v[54:57], v[74:77]
	v_mfma_f32_16x16x32_bf16 v[74:77], v[168:171], v[50:53], v[74:77]
	v_mfma_f32_16x16x32_bf16 v[74:77], v[172:175], v[46:49], v[74:77]
	v_mfma_f32_16x16x32_bf16 v[74:77], v[176:179], v[42:45], v[74:77]
	v_mfma_f32_16x16x32_bf16 v[74:77], v[180:183], v[38:41], v[74:77]
	v_mfma_f32_16x16x32_bf16 v[74:77], v[184:187], v[34:37], v[74:77]
	s_waitcnt lgkmcnt(0)
	v_mfma_f32_16x16x32_bf16 v[220:223], v[188:191], v[62:65], 0
	v_mfma_f32_16x16x32_bf16 v[220:223], v[192:195], v[58:61], v[220:223]
	v_mfma_f32_16x16x32_bf16 v[220:223], v[196:199], v[54:57], v[220:223]
	v_mfma_f32_16x16x32_bf16 v[220:223], v[200:203], v[50:53], v[220:223]
	v_mfma_f32_16x16x32_bf16 v[220:223], v[204:207], v[46:49], v[220:223]
	v_mfma_f32_16x16x32_bf16 v[220:223], v[208:211], v[42:45], v[220:223]
	v_mfma_f32_16x16x32_bf16 v[220:223], v[212:215], v[38:41], v[220:223]
	v_mfma_f32_16x16x32_bf16 v[220:223], v[216:219], v[34:37], v[220:223]
	s_nop 7
	v_cvt_pk_bf16_f32 v70, v70, s0
	v_cvt_pk_bf16_f32 v71, v71, s0
	v_cvt_pk_bf16_f32 v72, v72, s0
	v_cvt_pk_bf16_f32 v73, v73, s0
	v_cvt_pk_bf16_f32 v82, v66, s0
	v_cvt_pk_bf16_f32 v83, v67, s0
	v_cvt_pk_bf16_f32 v84, v68, s0
	v_cvt_pk_bf16_f32 v85, v69, s0
	v_lshlrev_b32_e32 v106, 2, v104
	v_cmp_gt_u32_e32 vcc, v106, v102
	v_cvt_pk_bf16_f32 v78, v74, s0
	v_or_b32_e32 v74, 3, v106
	v_cvt_pk_bf16_f32 v79, v75, s0
	s_nop 1
	v_mov_b32_e32 v66, v220
	v_mov_b32_e32 v67, v221
	v_mov_b32_e32 v68, v222
	v_mov_b32_e32 v69, v223
	v_cvt_pk_bf16_f32 v80, v76, s0
	v_cvt_pk_bf16_f32 v81, v77, s0
	v_cmp_gt_u32_e64 s[6:7], v74, v102
	v_cndmask_b32_e64 v75, v82, 0, vcc
	v_or_b32_e32 v120, 51, v106
	s_nop 2
	v_cvt_pk_bf16_f32 v89, v69, s0
	v_or_b32_e32 v69, 2, v106
	v_cvt_pk_bf16_f32 v66, v66, s0
	v_cvt_pk_bf16_f32 v67, v67, s0
	v_cvt_pk_bf16_f32 v68, v68, s0
	v_cmp_lt_u32_e64 s[0:1], v106, v102
	v_cmp_gt_u32_e64 s[4:5], v69, v102
	v_cndmask_b32_e64 v77, v85, 0, s[6:7]
	v_cndmask_b32_e64 v76, 0, v83, s[0:1]
	v_cndmask_b32_e64 v69, v84, 0, s[4:5]
	v_perm_b32 v74, v76, v75, s38
	v_perm_b32 v75, v77, v69, s38
	v_or_b32_e32 v69, 17, v106
	v_or_b32_e32 v76, 16, v106
	v_cmp_gt_u32_e64 s[8:9], v76, v102
	v_cmp_gt_u32_e64 s[10:11], v69, v102
	s_nop 0
	v_cndmask_b32_e64 v70, v70, 0, s[8:9]
	v_cndmask_b32_e64 v69, v71, 0, s[10:11]
	v_perm_b32 v76, v69, v70, s38
	v_or_b32_e32 v69, 19, v106
	v_or_b32_e32 v70, 18, v106
	v_cmp_gt_u32_e64 s[16:17], v70, v102
	v_cmp_gt_u32_e64 s[20:21], v69, v102
	v_or_b32_e32 v71, 35, v106
	v_cndmask_b32_e64 v70, v72, 0, s[16:17]
	v_cndmask_b32_e64 v69, v73, 0, s[20:21]
	v_perm_b32 v77, v69, v70, s38
	v_or_b32_e32 v69, 33, v106
	v_or_b32_e32 v70, 34, v106
	v_or_b32_e32 v72, 32, v106
	v_cmp_gt_u32_e64 s[12:13], v72, v102
	v_cmp_gt_u32_e64 s[14:15], v69, v102
	v_cmp_gt_u32_e64 s[18:19], v70, v102
	v_cmp_gt_u32_e64 s[22:23], v71, v102
	v_cndmask_b32_e64 v72, v78, 0, s[12:13]
	v_cndmask_b32_e64 v69, v79, 0, s[14:15]
	v_cndmask_b32_e64 v70, v80, 0, s[18:19]
	v_cndmask_b32_e64 v71, v81, 0, s[22:23]
	v_perm_b32 v86, v69, v72, s38
	v_perm_b32 v87, v71, v70, s38
	v_or_b32_e32 v69, 49, v106
	v_or_b32_e32 v70, 48, v106
	v_cmp_gt_u32_e64 s[24:25], v70, v102
	v_cmp_gt_u32_e64 s[26:27], v69, v102
	s_nop 0
	v_cndmask_b32_e64 v66, v66, 0, s[24:25]
	v_cndmask_b32_e64 v67, v67, 0, s[26:27]
	v_perm_b32 v88, v67, v66, s38
	v_or_b32_e32 v66, 50, v106
	v_cmp_gt_u32_e64 s[28:29], v66, v102
	v_lshrrev_b32_e32 v67, 1, v104
	v_bfe_u32 v66, v0, 1, 3
	v_cndmask_b32_e64 v121, v68, 0, s[28:29]
	v_lshrrev_b32_e32 v68, 1, v0
	v_bitop3_b32 v69, v67, v68, 7 bitop3:0x78
	v_and_b32_e32 v111, 8, v68
	v_lshlrev_b32_e32 v109, 4, v69
	v_add3_u32 v70, s30, v111, v112
	v_add_u32_e32 v128, v70, v109
	s_waitcnt vmcnt(9)
	s_barrier
	v_lshlrev_b32_e32 v2, 4, v104
	s_add_i32 s46, 0, 0x26000
	s_add_i32 s47, 0, 0x26100
	v_add_u32_e32 v3, s46, v2
	v_add_u32_e32 v4, s47, v2
	v_or_b32_e32 v5, 64, v2
	v_or_b32_e32 v7, 0x80, v2
	v_or_b32_e32 v2, 0xc0, v2
	v_add_u32_e32 v6, s46, v5
	v_add_u32_e32 v5, s47, v5
	v_add_u32_e32 v8, s46, v7
	v_add_u32_e32 v7, s47, v7
	v_add_u32_e32 v18, s46, v2
	v_add_u32_e32 v2, s47, v2
	ds_read_b128 v[30:33], v3
	ds_read_b128 v[14:17], v4
	ds_read_b128 v[26:29], v6
	ds_read_b128 v[10:13], v5
	ds_read_b128 v[22:25], v8
	ds_read_b128 v[6:9], v7
	ds_read_b128 v[18:21], v18
	ds_read_b128 v[2:5], v2
	ds_read2st64_b64 v[90:93], v128 offset1:4
	v_bitop3_b32 v68, v67, v66, 2 bitop3:0x36
	v_lshlrev_b32_e32 v110, 4, v68
	v_bitop3_b32 v71, v67, v66, 4 bitop3:0x36
	v_bitop3_b32 v72, v67, v66, 6 bitop3:0x36
	s_waitcnt lgkmcnt(0)
	v_mov_b32_e32 v82, v90
	v_add_u32_e32 v90, v70, v110
	ds_read2st64_b64 v[66:69], v90 offset1:4
	v_lshlrev_b32_e32 v107, 4, v71
	v_lshlrev_b32_e32 v108, 4, v72
	v_add_u32_e32 v136, v70, v107
	v_add_u32_e32 v140, v70, v108
	ds_read2st64_b64 v[94:97], v136 offset1:4
	ds_read2st64_b64 v[70:73], v140 offset1:4
	v_mov_b32_e32 v83, v91
	s_waitcnt lgkmcnt(0)
	v_mov_b32_e32 v84, v66
	v_mov_b32_e32 v85, v67
	v_mov_b32_e32 v78, v94
	v_mov_b32_e32 v79, v95
	v_mov_b32_e32 v80, v70
	v_mov_b32_e32 v81, v71
	v_mfma_f32_16x16x32_bf16 v[98:101], v[82:85], v[74:77], 0
	v_cmp_gt_u32_e64 s[30:31], v120, v102
	v_mov_b32_e32 v67, v93
	v_mov_b32_e32 v70, v96
	v_cndmask_b32_e64 v66, v89, 0, s[30:31]
	v_perm_b32 v89, v66, v121, s38
	v_mov_b32_e32 v66, v92
	ds_read_b128 v[120:123], v114 offset:32768
	ds_read_b128 v[124:127], v114 offset:40960
	v_mfma_f32_16x16x32_bf16 v[98:101], v[78:81], v[86:89], v[98:101]
	v_mov_b32_e32 v71, v97
	ds_read2st64_b64 v[128:131], v128 offset0:8 offset1:12
	ds_read2st64_b64 v[90:93], v90 offset0:8 offset1:12
	ds_read2st64_b64 v[136:139], v136 offset0:8 offset1:12
	s_waitcnt lgkmcnt(0)
	v_mfma_f32_16x16x32_bf16 v[120:123], v[120:123], v[62:65], v[98:101]
	v_mov_b32_e32 v94, v128
	v_mov_b32_e32 v95, v129
	v_mfma_f32_16x16x32_bf16 v[98:101], v[66:69], v[74:77], 0
	v_mov_b32_e32 v96, v90
	v_mov_b32_e32 v97, v91
	v_mov_b32_e32 v90, v130
	v_mfma_f32_16x16x32_bf16 v[132:135], v[70:73], v[86:89], v[98:101]
	v_mov_b32_e32 v91, v131
	s_nop 2
	ds_read2st64_b64 v[98:101], v140 offset0:8 offset1:12
	v_mfma_f32_16x16x32_bf16 v[124:127], v[124:127], v[62:65], v[132:135]
	ds_read_b128 v[144:147], v114 offset:49152
	ds_read_b128 v[148:151], v114 offset:57344
	ds_read_b128 v[128:131], v115 offset:32768
	v_mov_b32_e32 v132, v136
	v_mov_b32_e32 v133, v137
	s_waitcnt lgkmcnt(0)
	v_mov_b32_e32 v134, v98
	v_mov_b32_e32 v135, v99
	v_mov_b32_e32 v98, v138
	v_mov_b32_e32 v99, v139
	v_mfma_f32_16x16x32_bf16 v[140:143], v[94:97], v[74:77], 0
	v_mfma_f32_16x16x32_bf16 v[74:77], v[90:93], v[74:77], 0
	v_mfma_f32_16x16x32_bf16 v[140:143], v[132:135], v[86:89], v[140:143]
	v_mfma_f32_16x16x32_bf16 v[74:77], v[98:101], v[86:89], v[74:77]
	ds_read_b128 v[86:89], v117 offset:32768
	v_mfma_f32_16x16x32_bf16 v[140:143], v[144:147], v[62:65], v[140:143]
	v_mfma_f32_16x16x32_bf16 v[62:65], v[148:151], v[62:65], v[74:77]
	s_nop 4
	ds_read_b128 v[74:77], v117 offset:40960
	s_waitcnt lgkmcnt(0)
	v_mfma_f32_16x16x32_bf16 v[86:89], v[86:89], v[58:61], v[120:123]
	s_nop 2
	ds_read_b128 v[120:123], v117 offset:49152
	v_mfma_f32_16x16x32_bf16 v[74:77], v[74:77], v[58:61], v[124:127]
	s_nop 2
	ds_read_b128 v[124:127], v117 offset:57344
	s_waitcnt lgkmcnt(0)
	v_mfma_f32_16x16x32_bf16 v[120:123], v[120:123], v[58:61], v[140:143]
	v_mfma_f32_16x16x32_bf16 v[58:61], v[124:127], v[58:61], v[62:65]
	ds_read_b128 v[124:127], v115 offset:49152
	s_nop 1
	ds_read_b128 v[62:65], v115 offset:40960
	s_waitcnt lgkmcnt(0)
	v_mfma_f32_16x16x32_bf16 v[62:65], v[62:65], v[54:57], v[74:77]
	s_nop 2
	ds_read_b128 v[74:77], v115 offset:57344
	v_cndmask_b32_e64 v115, 0, 1.0, s[0:1]
	v_mfma_f32_16x16x32_bf16 v[120:123], v[124:127], v[54:57], v[120:123]
	ds_read_b128 v[124:127], v113 offset:32768
	v_mfma_f32_16x16x32_bf16 v[86:89], v[128:131], v[54:57], v[86:89]
	s_waitcnt lgkmcnt(0)
	v_mfma_f32_16x16x32_bf16 v[54:57], v[74:77], v[54:57], v[58:61]
	s_nop 2
	ds_read_b128 v[58:61], v113 offset:40960
	v_mfma_f32_16x16x32_bf16 v[74:77], v[124:127], v[50:53], v[86:89]
	s_nop 2
	ds_read_b128 v[86:89], v113 offset:49152
	s_waitcnt lgkmcnt(0)
	v_mfma_f32_16x16x32_bf16 v[58:61], v[58:61], v[50:53], v[62:65]
	s_nop 2
	ds_read_b128 v[62:65], v113 offset:57344
	v_mov_b32_e32 v113, 0x3f80
	v_cndmask_b32_e64 v114, v113, 0, vcc
	v_mfma_f32_16x16x32_bf16 v[86:89], v[86:89], v[50:53], v[120:123]
	s_nop 2
	ds_read_b128 v[120:123], v119 offset:32768
	s_waitcnt lgkmcnt(0)
	v_mfma_f32_16x16x32_bf16 v[50:53], v[62:65], v[50:53], v[54:57]
	s_nop 2
	ds_read_b128 v[54:57], v119 offset:40960
	v_mfma_f32_16x16x32_bf16 v[62:65], v[120:123], v[46:49], v[74:77]
	s_nop 2
	ds_read_b128 v[74:77], v119 offset:49152
	s_waitcnt lgkmcnt(0)
	v_mfma_f32_16x16x32_bf16 v[74:77], v[74:77], v[46:49], v[86:89]
	s_nop 2
	ds_read_b128 v[86:89], v118 offset:32768
	v_mfma_f32_16x16x32_bf16 v[54:57], v[54:57], v[46:49], v[58:61]
	s_nop 2
	ds_read_b128 v[58:61], v119 offset:57344
	s_waitcnt lgkmcnt(0)
	v_mfma_f32_16x16x32_bf16 v[46:49], v[58:61], v[46:49], v[50:53]
	s_nop 2
	ds_read_b128 v[50:53], v118 offset:40960
	v_mfma_f32_16x16x32_bf16 v[58:61], v[86:89], v[42:45], v[62:65]
	s_nop 2
	ds_read_b128 v[62:65], v118 offset:49152
	s_waitcnt lgkmcnt(0)
	v_mfma_f32_16x16x32_bf16 v[62:65], v[62:65], v[42:45], v[74:77]
	s_nop 2
	ds_read_b128 v[74:77], v116 offset:32768
	v_mfma_f32_16x16x32_bf16 v[50:53], v[50:53], v[42:45], v[54:57]
	s_nop 2
	ds_read_b128 v[54:57], v118 offset:57344
	s_waitcnt lgkmcnt(0)
	v_mfma_f32_16x16x32_bf16 v[42:45], v[54:57], v[42:45], v[46:49]
	s_nop 2
	ds_read_b128 v[46:49], v116 offset:40960
	ds_read_b128 v[54:57], v116 offset:49152
	ds_read_b128 v[86:89], v116 offset:57344
	v_cndmask_b32_e64 v116, v113, 0, s[4:5]
	v_mfma_f32_16x16x32_bf16 v[58:61], v[74:77], v[38:41], v[58:61]
	s_waitcnt lgkmcnt(0)
	v_mfma_f32_16x16x32_bf16 v[46:49], v[46:49], v[38:41], v[50:53]
	s_nop 2
	ds_read_b128 v[50:53], v1 offset:32768
	ds_read_b128 v[74:77], v1 offset:40960
	v_mfma_f32_16x16x32_bf16 v[54:57], v[54:57], v[38:41], v[62:65]
	v_mfma_f32_16x16x32_bf16 v[38:41], v[86:89], v[38:41], v[42:45]
	v_cndmask_b32_e64 v87, v113, 0, s[12:13]
	s_nop 0
	v_cndmask_b32_e64 v62, 1.0, 0, s[6:7]
	v_cndmask_b32_e64 v63, v113, 0, s[8:9]
	ds_read_b128 v[42:45], v1 offset:49152
	s_waitcnt lgkmcnt(0)
	v_mfma_f32_16x16x32_bf16 v[50:53], v[50:53], v[34:37], v[58:61]
	v_cndmask_b32_e64 v64, 1.0, 0, s[10:11]
	v_cndmask_b32_e64 v65, v113, 0, s[16:17]
	v_cndmask_b32_e64 v86, 1.0, 0, s[20:21]
	ds_read_b128 v[58:61], v1 offset:57344
	v_cndmask_b32_e64 v1, 1.0, 0, s[14:15]
	v_mfma_f32_16x16x32_bf16 v[46:49], v[74:77], v[34:37], v[46:49]
	v_cndmask_b32_e64 v74, v113, 0, s[18:19]
	v_cndmask_b32_e64 v75, 1.0, 0, s[22:23]
	v_cndmask_b32_e64 v76, v113, 0, s[24:25]
	v_mfma_f32_16x16x32_bf16 v[42:45], v[42:45], v[34:37], v[54:57]
	v_cndmask_b32_e64 v77, 1.0, 0, s[26:27]
	v_cndmask_b32_e64 v88, v113, 0, s[28:29]
	v_cndmask_b32_e64 v89, 1.0, 0, s[30:31]
	s_waitcnt lgkmcnt(0)
	v_mfma_f32_16x16x32_bf16 v[38:41], v[58:61], v[34:37], v[38:41]
	v_or_b32_e32 v34, v1, v87
	v_add3_u32 v1, s34, v111, v112
	v_add_u32_e32 v113, v1, v109
	v_add_u32_e32 v118, v1, v110
	v_or_b32_e32 v55, v62, v116
	v_or_b32_e32 v56, v64, v63
	v_or_b32_e32 v57, v86, v65
	v_or_b32_e32 v35, v75, v74
	ds_read2st64_b64 v[62:65], v113 offset1:4
	v_or_b32_e32 v36, v77, v76
	ds_read2st64_b64 v[74:77], v118 offset1:4
	v_add_u32_e32 v119, v1, v107
	v_add_u32_e32 v1, v1, v108
	v_or_b32_e32 v54, v115, v114
	v_or_b32_e32 v37, v89, v88
	ds_read2st64_b64 v[86:89], v119 offset1:4
	ds_read2st64_b64 v[114:117], v1 offset1:4
	v_mfma_f32_16x16x32_bf16 v[58:61], v[82:85], v[54:57], 0
	s_waitcnt lgkmcnt(0)
	v_mov_b32_e32 v82, v62
	v_mov_b32_e32 v83, v63
	v_mov_b32_e32 v84, v74
	v_mov_b32_e32 v85, v75
	v_mfma_f32_16x16x32_bf16 v[66:69], v[66:69], v[54:57], 0
	v_mov_b32_e32 v74, v64
	v_mov_b32_e32 v75, v65
	ds_read2st64_b64 v[62:65], v113 offset0:8 offset1:12
	v_mfma_f32_16x16x32_bf16 v[58:61], v[78:81], v[34:37], v[58:61]
	v_mov_b32_e32 v78, v86
	v_mov_b32_e32 v79, v87
	v_mov_b32_e32 v80, v114
	v_mov_b32_e32 v81, v115
	v_mfma_f32_16x16x32_bf16 v[82:85], v[82:85], v[54:57], 0
	v_mov_b32_e32 v114, v88
	v_mov_b32_e32 v115, v89
	v_mul_f32_e32 v51, 0x3d800000, v51
	v_mfma_f32_16x16x32_bf16 v[66:69], v[70:73], v[34:37], v[66:69]
	v_mul_f32_e32 v52, 0x3d800000, v52
	v_mul_f32_e32 v53, 0x3d800000, v53
	s_mov_b32 s34, 0xff61b1e6
	v_mfma_f32_16x16x32_bf16 v[70:73], v[94:97], v[54:57], 0
	v_mul_f32_e32 v46, 0x3d800000, v46
	s_nop 2
	v_add_f32_e32 v86, v66, v26
	v_add_f32_e32 v87, v67, v27
	v_mfma_f32_16x16x32_bf16 v[78:81], v[78:81], v[34:37], v[82:85]
	v_add_f32_e32 v94, v68, v28
	v_add_f32_e32 v95, v69, v29
	ds_read2st64_b64 v[66:69], v119 offset0:8 offset1:12
	v_add_f32_e32 v82, v58, v30
	v_add_f32_e32 v83, v59, v31
	v_add_f32_e32 v84, v60, v32
	v_add_f32_e32 v85, v61, v33
	v_mfma_f32_16x16x32_bf16 v[30:33], v[132:135], v[34:37], v[70:73]
	v_mul_f32_e32 v47, 0x3d800000, v47
	v_mul_f32_e32 v48, 0x3d800000, v48
	v_mul_f32_e32 v49, 0x3d800000, v49
	v_mfma_f32_16x16x32_bf16 v[26:29], v[90:93], v[54:57], 0
	ds_read2st64_b64 v[70:73], v1 offset0:8 offset1:12
	s_nop 2
	v_add_f32_e32 v90, v30, v22
	v_add_f32_e32 v91, v31, v23
	v_add_f32_e32 v92, v32, v24
	v_add_f32_e32 v88, v33, v25
	ds_read2st64_b64 v[22:25], v118 offset0:8 offset1:12
	v_mfma_f32_16x16x32_bf16 v[58:61], v[74:77], v[54:57], 0
	s_waitcnt lgkmcnt(0)
	v_mov_b32_e32 v74, v66
	v_mov_b32_e32 v75, v67
	v_mov_b32_e32 v76, v70
	v_mfma_f32_16x16x32_bf16 v[30:33], v[114:117], v[34:37], v[58:61]
	v_mov_b32_e32 v77, v71
	v_mov_b32_e32 v70, v68
	v_add_f32_e32 v68, v79, v15
	v_mov_b32_e32 v58, v62
	v_mov_b32_e32 v59, v63
	v_mov_b32_e32 v60, v22
	v_mov_b32_e32 v61, v23
	v_mfma_f32_16x16x32_bf16 v[26:29], v[98:101], v[34:37], v[26:29]
	v_rcp_f32_e32 v62, v85
	v_rcp_f32_e32 v63, v86
	v_rcp_f32_e32 v79, v87
	v_mfma_f32_16x16x32_bf16 v[58:61], v[58:61], v[54:57], 0
	v_mov_b32_e32 v71, v69
	s_nop 2
	v_add_f32_e32 v26, v26, v18
	v_add_f32_e32 v1, v27, v19
	v_add_f32_e32 v27, v28, v20
	v_add_f32_e32 v28, v29, v21
	v_mfma_f32_16x16x32_bf16 v[18:21], v[74:77], v[34:37], v[58:61]
	v_mul_f32_e32 v29, 0x3d800000, v50
	v_rcp_f32_e32 v50, v82
	v_add_f32_e32 v69, v80, v16
	v_rcp_f32_e32 v60, v83
	v_rcp_f32_e32 v61, v84
	v_add_f32_e32 v74, v81, v17
	v_rcp_f32_e32 v80, v94
	v_rcp_f32_e32 v81, v95
	v_add_f32_e32 v75, v30, v10
	v_add_f32_e32 v76, v31, v11
	v_mul_f32_e32 v30, 0x3d800000, v42
	v_mul_f32_e32 v31, 0x3d800000, v43
	v_add_f32_e32 v42, v18, v6
	v_add_f32_e32 v43, v19, v7
	v_mul_f32_e32 v18, v29, v50
	v_mul_f32_e32 v19, v51, v60
	v_rcp_f32_e32 v82, v90
	v_rcp_f32_e32 v83, v91
	v_add_f32_e32 v77, v32, v12
	v_mul_f32_e32 v32, 0x3d800000, v44
	v_add_f32_e32 v44, v20, v8
	v_max3_f32 v18, v18, s34, v19
	v_mul_f32_e32 v19, v52, v61
	v_mul_f32_e32 v20, v53, v62
	v_rcp_f32_e32 v84, v92
	v_rcp_f32_e32 v85, v88
	v_max3_f32 v18, v18, v19, v20
	v_mul_f32_e32 v19, v46, v63
	v_mul_f32_e32 v20, v47, v79
	v_rcp_f32_e32 v86, v26
	v_rcp_f32_e32 v87, v1
	v_max3_f32 v18, v18, v19, v20
	v_mul_f32_e32 v19, v48, v80
	v_mul_f32_e32 v20, v49, v81
	v_rcp_f32_e32 v88, v27
	v_rcp_f32_e32 v89, v28
	v_add_f32_e32 v67, v78, v14
	v_add_f32_e32 v78, v33, v13
	v_mul_f32_e32 v33, 0x3d800000, v45
	v_max3_f32 v18, v18, v19, v20
	v_mul_f32_e32 v19, v30, v82
	v_mul_f32_e32 v20, v31, v83
	v_max3_f32 v18, v18, v19, v20
	v_mul_f32_e32 v19, v32, v84
	v_mul_f32_e32 v20, v33, v85
	v_mul_f32_e32 v38, 0x3d800000, v38
	v_mul_f32_e32 v39, 0x3d800000, v39
	v_max3_f32 v18, v18, v19, v20
	v_mul_f32_e32 v1, v38, v86
	v_mul_f32_e32 v19, v39, v87
	v_mul_f32_e32 v40, 0x3d800000, v40
	v_mul_f32_e32 v41, 0x3d800000, v41
	v_max3_f32 v1, v18, v1, v19
	v_mul_f32_e32 v18, v40, v88
	v_mul_f32_e32 v19, v41, v89
	v_max3_f32 v1, v1, v18, v19
	v_mbcnt_lo_u32_b32 v18, -1, 0
	v_mbcnt_hi_u32_b32 v26, -1, v18
	v_and_b32_e32 v19, 64, v26
	v_xor_b32_e32 v18, 16, v26
	v_add_u32_e32 v27, 64, v19
	v_cmp_lt_i32_e64 s[34:35], v18, v27
	v_mov_b32_e32 v22, v64
	v_mov_b32_e32 v23, v65
	v_cndmask_b32_e64 v18, v26, v18, s[34:35]
	v_lshlrev_b32_e32 v64, 2, v18
	ds_bpermute_b32 v28, v64, v1
	v_add_f32_e32 v45, v21, v9
	v_mfma_f32_16x16x32_bf16 v[18:21], v[22:25], v[54:57], 0
	v_lshlrev_b32_e32 v58, 9, v102
	v_mov_b32_e32 v59, 0
	s_waitcnt lgkmcnt(0)
	v_max_f32_e32 v24, v28, v28
	v_max_f32_e32 v24, v1, v24
	v_xor_b32_e32 v1, 32, v26
	v_cmp_lt_i32_e64 s[34:35], v1, v27
	v_lshl_add_u64 v[22:23], s[36:37], 0, v[58:59]
	v_lshlrev_b32_e32 v58, 3, v104
	v_cndmask_b32_e64 v1, v26, v1, s[34:35]
	v_lshlrev_b32_e32 v65, 2, v1
	ds_bpermute_b32 v25, v65, v24
	v_lshl_add_u64 v[22:23], v[22:23], 0, v[58:59]
	v_and_b32_e32 v58, 0x100, v0
	v_lshrrev_b32_e32 v66, 8, v0
	v_lshl_add_u64 v[0:1], v[22:23], 0, v[58:59]
	s_waitcnt lgkmcnt(0)
	v_max_f32_e32 v22, v25, v25
	v_max_f32_e32 v54, v24, v22
	v_fma_f32 v22, v29, v50, -v54
	v_mul_f32_e32 v22, 0x3fb8aa3b, v22
	v_fma_f32 v23, v51, v60, -v54
	v_exp_f32_e32 v22, v22
	v_mul_f32_e32 v23, 0x3fb8aa3b, v23
	v_fma_f32 v24, v52, v61, -v54
	v_exp_f32_e32 v23, v23
	v_mul_f32_e32 v24, 0x3fb8aa3b, v24
	v_fma_f32 v25, v53, v62, -v54
	v_exp_f32_e32 v24, v24
	v_mul_f32_e32 v25, 0x3fb8aa3b, v25
	v_fma_f32 v26, v46, v63, -v54
	v_exp_f32_e32 v25, v25
	v_mul_f32_e32 v26, 0x3fb8aa3b, v26
	v_fma_f32 v27, v47, v79, -v54
	v_exp_f32_e32 v26, v26
	v_mul_f32_e32 v27, 0x3fb8aa3b, v27
	v_fma_f32 v28, v48, v80, -v54
	v_add_f32_e32 v46, 0, v22
	v_exp_f32_e32 v27, v27
	v_mul_f32_e32 v28, 0x3fb8aa3b, v28
	v_fma_f32 v29, v49, v81, -v54
	v_add_f32_e32 v46, v46, v23
	v_exp_f32_e32 v28, v28
	v_mul_f32_e32 v29, 0x3fb8aa3b, v29
	v_add_f32_e32 v46, v46, v24
	v_fma_f32 v30, v30, v82, -v54
	v_exp_f32_e32 v29, v29
	v_add_f32_e32 v46, v46, v25
	v_mul_f32_e32 v30, 0x3fb8aa3b, v30
	v_fma_f32 v31, v31, v83, -v54
	v_add_f32_e32 v46, v46, v26
	v_exp_f32_e32 v30, v30
	v_mul_f32_e32 v31, 0x3fb8aa3b, v31
	v_fma_f32 v32, v32, v84, -v54
	v_add_f32_e32 v46, v46, v27
	v_exp_f32_e32 v31, v31
	v_mul_f32_e32 v32, 0x3fb8aa3b, v32
	v_fma_f32 v33, v33, v85, -v54
	v_add_f32_e32 v46, v46, v28
	v_exp_f32_e32 v32, v32
	v_mul_f32_e32 v33, 0x3fb8aa3b, v33
	v_fma_f32 v38, v38, v86, -v54
	v_add_f32_e32 v46, v46, v29
	v_exp_f32_e32 v33, v33
	v_mul_f32_e32 v38, 0x3fb8aa3b, v38
	v_fma_f32 v39, v39, v87, -v54
	v_add_f32_e32 v46, v46, v30
	v_exp_f32_e32 v38, v38
	v_mul_f32_e32 v39, 0x3fb8aa3b, v39
	v_fma_f32 v40, v40, v88, -v54
	v_add_f32_e32 v46, v46, v31
	v_exp_f32_e32 v39, v39
	v_mul_f32_e32 v40, 0x3fb8aa3b, v40
	v_fma_f32 v41, v41, v89, -v54
	v_add_f32_e32 v46, v46, v32
	v_exp_f32_e32 v40, v40
	v_mul_f32_e32 v41, 0x3fb8aa3b, v41
	v_add_f32_e32 v46, v46, v33
	v_exp_f32_e32 v41, v41
	v_add_f32_e32 v46, v46, v38
	v_add_f32_e32 v46, v46, v39
	v_add_f32_e32 v46, v46, v40
	v_add_f32_e32 v58, v46, v41
	ds_bpermute_b32 v79, v64, v58
	global_load_dwordx2 v[62:63], v[0:1], off
	global_load_dwordx2 v[60:61], v[0:1], off offset:32
	global_load_dwordx2 v[56:57], v[0:1], off offset:64
	global_load_dwordx2 v[52:53], v[0:1], off offset:96
	global_load_dwordx2 v[54:55], v[0:1], off offset:128
	global_load_dwordx2 v[50:51], v[0:1], off offset:160
	global_load_dwordx2 v[48:49], v[0:1], off offset:192
	global_load_dwordx2 v[46:47], v[0:1], off offset:224
	v_mfma_f32_16x16x32_bf16 v[18:21], v[70:73], v[34:37], v[18:21]
	v_rcp_f32_e32 v34, v75
	s_waitcnt lgkmcnt(0)
	v_add_f32_e32 v0, v58, v79
	ds_bpermute_b32 v1, v65, v0
	v_rcp_f32_e32 v35, v76
	v_rcp_f32_e32 v36, v77
	s_nop 1
	v_add_f32_e32 v58, v18, v2
	v_rcp_f32_e32 v18, v67
	s_waitcnt lgkmcnt(0)
	v_add_f32_e32 v0, v0, v1
	v_rcp_f32_e32 v0, v0
	v_add_f32_e32 v1, v19, v3
	v_rcp_f32_e32 v19, v68
	v_add_f32_e32 v70, v20, v4
	v_add_f32_e32 v71, v21, v5
	v_rcp_f32_e32 v20, v69
	v_rcp_f32_e32 v21, v74
	v_mul_f32_e32 v0, 0x43800000, v0
	v_pk_mul_f32 v[22:23], v[0:1], v[22:23] op_sel_hi:[0,1]
	v_pk_mul_f32 v[18:19], v[22:23], v[18:19]
	v_pk_mul_f32 v[22:23], v[0:1], v[24:25] op_sel_hi:[0,1]
	v_pk_mul_f32 v[20:21], v[22:23], v[20:21]
	v_rcp_f32_e32 v37, v78
	v_pk_mul_f32 v[14:15], v[14:15], v[18:19]
	v_pk_mul_f32 v[16:17], v[16:17], v[20:21]
	v_cvt_pk_f16_f32 v14, v14, v15
	v_cvt_pk_f16_f32 v15, v16, v17
	v_pk_mul_f32 v[16:17], v[0:1], v[26:27] op_sel_hi:[0,1]
	v_pk_mul_f32 v[16:17], v[16:17], v[34:35]
	v_cvt_pk_bf16_f32 v18, v18, v19
	v_cvt_pk_bf16_f32 v19, v20, v21
	v_pk_mul_f32 v[10:11], v[10:11], v[16:17]
	v_cvt_pk_bf16_f32 v20, v16, v17
	v_pk_mul_f32 v[16:17], v[0:1], v[28:29] op_sel_hi:[0,1]
	v_pk_mul_f32 v[72:73], v[16:17], v[36:37]
	v_rcp_f32_e32 v16, v42
	v_rcp_f32_e32 v17, v43
	v_rcp_f32_e32 v24, v44
	v_rcp_f32_e32 v25, v45
	v_rcp_f32_e32 v26, v58
	v_rcp_f32_e32 v27, v1
	v_pk_mul_f32 v[22:23], v[0:1], v[30:31] op_sel_hi:[0,1]
	v_pk_mul_f32 v[76:77], v[22:23], v[16:17]
	v_pk_mul_f32 v[16:17], v[0:1], v[32:33] op_sel_hi:[0,1]
	v_pk_mul_f32 v[78:79], v[16:17], v[24:25]
	v_pk_mul_f32 v[16:17], v[0:1], v[38:39] op_sel_hi:[0,1]
	s_add_i32 s34, 0, 0x24000
	v_pk_mul_f32 v[80:81], v[16:17], v[26:27]
	v_add3_u32 v16, s34, v112, v111
	v_add_u32_e32 v17, v16, v109
	v_add_u32_e32 v58, v16, v110
	s_barrier
	ds_write_b128 v152, v[70:73]
	ds_write_b128 v152, v[76:79] offset:1024
	ds_write_b64 v153, v[0:1] offset:2048
	ds_write_b64 v153, v[10:11] offset:2560
	ds_write_b64 v153, v[14:15] offset:3072
	ds_write_b64 v153, v[18:19] offset:3584
	ds_write_b64 v153, v[40:41] offset:4096
	ds_write_b64 v153, v[80:81] offset:4608
	ds_write_b32 v154, v20 offset:5120
	s_waitcnt lgkmcnt(0)
	s_branch .Lat_join
.Lat_dh1:
	s_waitcnt vmcnt(9)
	s_barrier
	v_lshlrev_b32_e32 v2, 4, v104
	s_add_i32 s46, 0, 0x26000
	s_add_i32 s47, 0, 0x26100
	v_add_u32_e32 v3, s46, v2
	v_add_u32_e32 v4, s47, v2
	v_or_b32_e32 v5, 64, v2
	v_or_b32_e32 v7, 0x80, v2
	v_or_b32_e32 v2, 0xc0, v2
	v_add_u32_e32 v6, s46, v5
	v_add_u32_e32 v5, s47, v5
	v_add_u32_e32 v8, s46, v7
	v_add_u32_e32 v7, s47, v7
	v_add_u32_e32 v18, s46, v2
	v_add_u32_e32 v2, s47, v2
	ds_read_b128 v[30:33], v3
	ds_read_b128 v[14:17], v4
	ds_read_b128 v[26:29], v6
	ds_read_b128 v[10:13], v5
	ds_read_b128 v[22:25], v8
	ds_read_b128 v[6:9], v7
	ds_read_b128 v[18:21], v18
	ds_read_b128 v[2:5], v2
	s_waitcnt lgkmcnt(0)
	s_add_u32 s36, s30, s34
	s_addc_u32 s37, s31, s35
	v_lshlrev_b32_e32 v112, 7, v103
	v_lshlrev_b32_e32 v106, 2, v104
	v_cmp_gt_u32_e32 vcc, v106, v102
	s_nop 1
	v_or_b32_e32 v74, 3, v106
	v_cmp_gt_u32_e64 s[6:7], v74, v102
	s_nop 1
	v_or_b32_e32 v120, 51, v106
	v_or_b32_e32 v69, 2, v106
	v_cmp_lt_u32_e64 s[0:1], v106, v102
	s_nop 1
	v_cmp_gt_u32_e64 s[4:5], v69, v102
	s_nop 1
	v_or_b32_e32 v69, 17, v106
	v_or_b32_e32 v76, 16, v106
	v_cmp_gt_u32_e64 s[8:9], v76, v102
	s_nop 1
	v_cmp_gt_u32_e64 s[10:11], v69, v102
	s_nop 1
	v_or_b32_e32 v69, 19, v106
	v_or_b32_e32 v70, 18, v106
	v_cmp_gt_u32_e64 s[16:17], v70, v102
	s_nop 1
	v_cmp_gt_u32_e64 s[20:21], v69, v102
	s_nop 1
	v_or_b32_e32 v71, 35, v106
	v_or_b32_e32 v69, 33, v106
	v_or_b32_e32 v70, 34, v106
	v_or_b32_e32 v72, 32, v106
	v_cmp_gt_u32_e64 s[12:13], v72, v102
	s_nop 1
	v_cmp_gt_u32_e64 s[14:15], v69, v102
	s_nop 1
	v_cmp_gt_u32_e64 s[18:19], v70, v102
	s_nop 1
	v_cmp_gt_u32_e64 s[22:23], v71, v102
	s_nop 1
	v_or_b32_e32 v69, 49, v106
	v_or_b32_e32 v70, 48, v106
	v_cmp_gt_u32_e64 s[24:25], v70, v102
	s_nop 1
	v_cmp_gt_u32_e64 s[26:27], v69, v102
	s_nop 1
	v_or_b32_e32 v66, 50, v106
	v_cmp_gt_u32_e64 s[28:29], v66, v102
	s_nop 1
	v_lshrrev_b32_e32 v67, 1, v104
	v_bfe_u32 v66, v0, 1, 3
	v_lshrrev_b32_e32 v68, 1, v0
	v_bitop3_b32 v69, v67, v68, 7 bitop3:0x78
	v_and_b32_e32 v111, 8, v68
	v_lshlrev_b32_e32 v109, 4, v69
	v_bitop3_b32 v68, v67, v66, 2 bitop3:0x36
	v_lshlrev_b32_e32 v110, 4, v68
	v_bitop3_b32 v71, v67, v66, 4 bitop3:0x36
	v_bitop3_b32 v72, v67, v66, 6 bitop3:0x36
	v_lshlrev_b32_e32 v107, 4, v71
	v_lshlrev_b32_e32 v108, 4, v72
	v_cmp_gt_u32_e64 s[30:31], v120, v102
	s_nop 1
	v_mbcnt_lo_u32_b32 v18, -1, 0
	v_mbcnt_hi_u32_b32 v26, -1, v18
	v_and_b32_e32 v19, 64, v26
	v_xor_b32_e32 v18, 16, v26
	v_add_u32_e32 v27, 64, v19
	v_cmp_lt_i32_e64 s[34:35], v18, v27
	s_nop 1
	v_cndmask_b32_e64 v18, v26, v18, s[34:35]
	v_lshlrev_b32_e32 v64, 2, v18
	v_lshlrev_b32_e32 v58, 9, v102
	v_mov_b32_e32 v59, 0
	v_xor_b32_e32 v1, 32, v26
	v_cmp_lt_i32_e64 s[34:35], v1, v27
	s_nop 1
	v_lshl_add_u64 v[22:23], s[36:37], 0, v[58:59]
	v_lshlrev_b32_e32 v58, 3, v104
	v_cndmask_b32_e64 v1, v26, v1, s[34:35]
	v_lshlrev_b32_e32 v65, 2, v1
	v_lshl_add_u64 v[22:23], v[22:23], 0, v[58:59]
	v_and_b32_e32 v58, 0x100, v0
	v_lshrrev_b32_e32 v66, 8, v0
	v_lshl_add_u64 v[0:1], v[22:23], 0, v[58:59]
	global_load_dwordx2 v[62:63], v[0:1], off
	global_load_dwordx2 v[60:61], v[0:1], off offset:32
	global_load_dwordx2 v[56:57], v[0:1], off offset:64
	global_load_dwordx2 v[52:53], v[0:1], off offset:96
	global_load_dwordx2 v[54:55], v[0:1], off offset:128
	global_load_dwordx2 v[50:51], v[0:1], off offset:160
	global_load_dwordx2 v[48:49], v[0:1], off offset:192
	global_load_dwordx2 v[46:47], v[0:1], off offset:224
	s_add_i32 s34, 0, 0x24000
	v_add3_u32 v16, s34, v112, v111
	v_add_u32_e32 v17, v16, v109
	v_add_u32_e32 v58, v16, v110
	s_barrier

	.amdhsa_kernel _Z9attn_fastPKtS0_S0_S0_S0_S0_S0_S0_S0_PKfS2_Pt
		.amdhsa_group_segment_fixed_size 0
		.amdhsa_private_segment_fixed_size 0
		.amdhsa_kernarg_size 96
		.amdhsa_user_sgpr_count 2
		.amdhsa_user_sgpr_dispatch_ptr 0
		.amdhsa_user_sgpr_queue_ptr 0
		.amdhsa_user_sgpr_kernarg_segment_ptr 1
		.amdhsa_user_sgpr_dispatch_id 0
		.amdhsa_user_sgpr_kernarg_preload_length 0
		.amdhsa_user_sgpr_kernarg_preload_offset 0
		.amdhsa_user_sgpr_private_segment_size 0
		.amdhsa_uses_dynamic_stack 0
		.amdhsa_enable_private_segment 0
		.amdhsa_system_sgpr_workgroup_id_x 1
		.amdhsa_system_sgpr_workgroup_id_y 0
		.amdhsa_system_sgpr_workgroup_id_z 0
		.amdhsa_system_sgpr_workgroup_info 0
		.amdhsa_system_vgpr_workitem_id 0
		.amdhsa_next_free_vgpr 224
		.amdhsa_next_free_sgpr 48
		.amdhsa_accum_offset 224
		.amdhsa_reserve_vcc 1
		.amdhsa_float_round_mode_32 0
		.amdhsa_float_round_mode_16_64 0
		.amdhsa_float_denorm_mode_32 3
		.amdhsa_float_denorm_mode_16_64 3
		.amdhsa_dx10_clamp 1
		.amdhsa_ieee_mode 1
		.amdhsa_fp16_overflow 0
		.amdhsa_tg_split 0
		.amdhsa_exception_fp_ieee_invalid_op 0
		.amdhsa_exception_fp_denorm_src 0
		.amdhsa_exception_fp_ieee_div_zero 0
		.amdhsa_exception_fp_ieee_overflow 0
		.amdhsa_exception_fp_ieee_underflow 0
		.amdhsa_exception_fp_ieee_inexact 0
		.amdhsa_exception_int_div_zero 0
	.end_amdhsa_kernel

amdhsa.kernels:
  - .agpr_count:     0
    .args:
      - .actual_access:  read_only
        .address_space:  global
        .offset:         0
        .size:           8
        .value_kind:     global_buffer
      - .actual_access:  read_only
        .address_space:  global
        .offset:         8
        .size:           8
        .value_kind:     global_buffer
      - .actual_access:  write_only
        .address_space:  global
        .offset:         16
        .size:           8
        .value_kind:     global_buffer
      - .offset:         24
        .size:           4
        .value_kind:     by_value
      - .offset:         28
        .size:           4
        .value_kind:     by_value
      - .offset:         32
        .size:           4
        .value_kind:     by_value
      - .offset:         36
        .size:           4
        .value_kind:     by_value
    .group_segment_fixed_size: 8256
    .kernarg_segment_align: 8
    .kernarg_segment_size: 40
    .language:       OpenCL C
    .language_version:
      - 2
      - 0
    .max_flat_workgroup_size: 256
    .name:           _Z14gemm_f32_naivePKfS0_Pfiiii
    .private_segment_fixed_size: 0
    .sgpr_count:     24
    .sgpr_spill_count: 0
    .symbol:         _Z14gemm_f32_naivePKfS0_Pfiiii.kd
    .uniform_work_group_size: 1
    .uses_dynamic_stack: false
    .vgpr_count:     76
    .vgpr_spill_count: 0
    .wavefront_size: 64
  - .agpr_count:     0
    .args:
      - .actual_access:  read_only
        .address_space:  global
        .offset:         0
        .size:           8
        .value_kind:     global_buffer
      - .actual_access:  write_only
        .address_space:  global
        .offset:         8
        .size:           8
        .value_kind:     global_buffer
      - .actual_access:  write_only
        .address_space:  global
        .offset:         16
        .size:           8
        .value_kind:     global_buffer
      - .actual_access:  write_only
        .address_space:  global
        .offset:         24
        .size:           8
        .value_kind:     global_buffer
      - .actual_access:  write_only
        .address_space:  global
        .offset:         32
        .size:           8
        .value_kind:     global_buffer
      - .actual_access:  write_only
        .address_space:  global
        .offset:         40
        .size:           8
        .value_kind:     global_buffer
      - .actual_access:  write_only
        .address_space:  global
        .offset:         48
        .size:           8
        .value_kind:     global_buffer
    .group_segment_fixed_size: 0
    .kernarg_segment_align: 8
    .kernarg_segment_size: 56
    .language:       OpenCL C
    .language_version:
      - 2
      - 0
    .max_flat_workgroup_size: 256
    .name:           _Z10post_naivePKfPtS1_S1_S1_S1_S1_
    .private_segment_fixed_size: 0
    .sgpr_count:     28
    .sgpr_spill_count: 0
    .symbol:         _Z10post_naivePKfPtS1_S1_S1_S1_S1_.kd
    .uniform_work_group_size: 1
    .uses_dynamic_stack: false
    .vgpr_count:     38
    .vgpr_spill_count: 0
    .wavefront_size: 64
  - .agpr_count:     0
    .args:
      - .actual_access:  read_only
        .address_space:  global
        .offset:         0
        .size:           8
        .value_kind:     global_buffer
      - .actual_access:  read_only
        .address_space:  global
        .offset:         8
        .size:           8
        .value_kind:     global_buffer
      - .actual_access:  read_only
        .address_space:  global
        .offset:         16
        .size:           8
        .value_kind:     global_buffer
      - .actual_access:  read_only
        .address_space:  global
        .offset:         24
        .size:           8
        .value_kind:     global_buffer
      - .actual_access:  read_only
        .address_space:  global
        .offset:         32
        .size:           8
        .value_kind:     global_buffer
      - .actual_access:  read_only
        .address_space:  global
        .offset:         40
        .size:           8
        .value_kind:     global_buffer
      - .actual_access:  read_only
        .address_space:  global
        .offset:         48
        .size:           8
        .value_kind:     global_buffer
      - .actual_access:  write_only
        .address_space:  global
        .offset:         56
        .size:           8
        .value_kind:     global_buffer
      - .actual_access:  write_only
        .address_space:  global
        .offset:         64
        .size:           8
        .value_kind:     global_buffer
      - .actual_access:  write_only
        .address_space:  global
        .offset:         72
        .size:           8
        .value_kind:     global_buffer
      - .actual_access:  write_only
        .address_space:  global
        .offset:         80
        .size:           8
        .value_kind:     global_buffer
    .group_segment_fixed_size: 1152
    .kernarg_segment_align: 8
    .kernarg_segment_size: 88
    .language:       OpenCL C
    .language_version:
      - 2
      - 0
    .max_flat_workgroup_size: 256
    .name:           _Z11gates_naivePKfS0_S0_S0_S0_S0_S0_PtS1_S1_S1_
    .private_segment_fixed_size: 0
    .sgpr_count:     32
    .sgpr_spill_count: 0
    .symbol:         _Z11gates_naivePKfS0_S0_S0_S0_S0_S0_PtS1_S1_S1_.kd
    .uniform_work_group_size: 1
    .uses_dynamic_stack: false
    .vgpr_count:     66
    .vgpr_spill_count: 0
    .wavefront_size: 64
  - .agpr_count:     0
    .args:
      - .actual_access:  read_only
        .address_space:  global
        .offset:         0
        .size:           8
        .value_kind:     global_buffer
      - .actual_access:  read_only
        .address_space:  global
        .offset:         8
        .size:           8
        .value_kind:     global_buffer
      - .actual_access:  read_only
        .address_space:  global
        .offset:         16
        .size:           8
        .value_kind:     global_buffer
      - .actual_access:  read_only
        .address_space:  global
        .offset:         24
        .size:           8
        .value_kind:     global_buffer
      - .actual_access:  read_only
        .address_space:  global
        .offset:         32
        .size:           8
        .value_kind:     global_buffer
      - .actual_access:  read_only
        .address_space:  global
        .offset:         40
        .size:           8
        .value_kind:     global_buffer
      - .actual_access:  read_only
        .address_space:  global
        .offset:         48
        .size:           8
        .value_kind:     global_buffer
      - .actual_access:  write_only
        .address_space:  global
        .offset:         56
        .size:           8
        .value_kind:     global_buffer
    .group_segment_fixed_size: 12560
    .kernarg_segment_align: 8
    .kernarg_segment_size: 64
    .language:       OpenCL C
    .language_version:
      - 2
      - 0
    .max_flat_workgroup_size: 256
    .name:           _Z10attn_naivePKtS0_S0_S0_S0_S0_PKfPf
    .private_segment_fixed_size: 0
    .sgpr_count:     33
    .sgpr_spill_count: 0
    .symbol:         _Z10attn_naivePKtS0_S0_S0_S0_S0_PKfPf.kd
    .uniform_work_group_size: 1
    .uses_dynamic_stack: false
    .vgpr_count:     82
    .vgpr_spill_count: 0
    .wavefront_size: 64
  - .agpr_count:     0
    .args:
      - .address_space:  global
        .offset:         0
        .size:           8
        .value_kind:     global_buffer
      - .address_space:  global
        .offset:         8
        .size:           8
        .value_kind:     global_buffer
      - .actual_access:  write_only
        .address_space:  global
        .offset:         16
        .size:           8
        .value_kind:     global_buffer
    .group_segment_fixed_size: 0
    .kernarg_segment_align: 8
    .kernarg_segment_size: 24
    .language:       OpenCL C
    .language_version:
      - 2
      - 0
    .max_flat_workgroup_size: 512
    .name:           _Z8gemm_outPKtS0_Pf
    .private_segment_fixed_size: 0
    .sgpr_count:     26
    .sgpr_spill_count: 0
    .symbol:         _Z8gemm_outPKtS0_Pf.kd
    .uniform_work_group_size: 1
    .uses_dynamic_stack: false
    .vgpr_count:     158
    .vgpr_spill_count: 0
    .wavefront_size: 64
  - .agpr_count:     0
    .args:
      - .address_space:  global
        .offset:         0
        .size:           8
        .value_kind:     global_buffer
      - .address_space:  global
        .offset:         8
        .size:           8
        .value_kind:     global_buffer
      - .actual_access:  write_only
        .address_space:  global
        .offset:         16
        .size:           8
        .value_kind:     global_buffer
    .group_segment_fixed_size: 0
    .kernarg_segment_align: 8
    .kernarg_segment_size: 24
    .language:       OpenCL C
    .language_version:
      - 2
      - 0
    .max_flat_workgroup_size: 512
    .name:           _Z9gemm_out2PKtS0_Pf
    .private_segment_fixed_size: 0
    .sgpr_count:     27
    .sgpr_spill_count: 0
    .symbol:         _Z9gemm_out2PKtS0_Pf.kd
    .uniform_work_group_size: 1
    .uses_dynamic_stack: false
    .vgpr_count:     146
    .vgpr_spill_count: 0
    .wavefront_size: 64
  - .agpr_count:     0
    .args:
      - .actual_access:  read_only
        .address_space:  global
        .offset:         0
        .size:           8
        .value_kind:     global_buffer
      - .actual_access:  write_only
        .address_space:  global
        .offset:         8
        .size:           8
        .value_kind:     global_buffer
    .group_segment_fixed_size: 0
    .kernarg_segment_align: 8
    .kernarg_segment_size: 16
    .language:       OpenCL C
    .language_version:
      - 2
      - 0
    .max_flat_workgroup_size: 256
    .name:           _Z6conv_xPKfPt
    .private_segment_fixed_size: 0
    .sgpr_count:     14
    .sgpr_spill_count: 0
    .symbol:         _Z6conv_xPKfPt.kd
    .uniform_work_group_size: 1
    .uses_dynamic_stack: false
    .vgpr_count:     12
    .vgpr_spill_count: 0
    .wavefront_size: 64
  - .agpr_count:     0
    .args:
      - .actual_access:  read_only
        .address_space:  global
        .offset:         0
        .size:           8
        .value_kind:     global_buffer
      - .actual_access:  read_only
        .address_space:  global
        .offset:         8
        .size:           8
        .value_kind:     global_buffer
      - .actual_access:  read_only
        .address_space:  global
        .offset:         16
        .size:           8
        .value_kind:     global_buffer
      - .actual_access:  read_only
        .address_space:  global
        .offset:         24
        .size:           8
        .value_kind:     global_buffer
      - .actual_access:  read_only
        .address_space:  global
        .offset:         32
        .size:           8
        .value_kind:     global_buffer
      - .actual_access:  write_only
        .address_space:  global
        .offset:         40
        .size:           8
        .value_kind:     global_buffer
      - .actual_access:  write_only
        .address_space:  global
        .offset:         48
        .size:           8
        .value_kind:     global_buffer
    .group_segment_fixed_size: 16640
    .kernarg_segment_align: 8
    .kernarg_segment_size: 56
    .language:       OpenCL C
    .language_version:
      - 2
      - 0
    .max_flat_workgroup_size: 256
    .name:           _Z7conv_wTPKfS0_S0_S0_S0_PtS1_
    .private_segment_fixed_size: 0
    .sgpr_count:     26
    .sgpr_spill_count: 0
    .symbol:         _Z7conv_wTPKfS0_S0_S0_S0_PtS1_.kd
    .uniform_work_group_size: 1
    .uses_dynamic_stack: false
    .vgpr_count:     51
    .vgpr_spill_count: 0
    .wavefront_size: 64
  - .agpr_count:     0
    .args:
      - .actual_access:  read_only
        .address_space:  global
        .offset:         0
        .size:           8
        .value_kind:     global_buffer
      - .actual_access:  read_only
        .address_space:  global
        .offset:         8
        .size:           8
        .value_kind:     global_buffer
      - .actual_access:  write_only
        .address_space:  global
        .offset:         16
        .size:           8
        .value_kind:     global_buffer
    .group_segment_fixed_size: 0
    .kernarg_segment_align: 8
    .kernarg_segment_size: 24
    .language:       OpenCL C
    .language_version:
      - 2
      - 0
    .max_flat_workgroup_size: 256
    .name:           _Z7conv_w1PKfS0_Pt
    .private_segment_fixed_size: 0
    .sgpr_count:     16
    .sgpr_spill_count: 0
    .symbol:         _Z7conv_w1PKfS0_Pt.kd
    .uniform_work_group_size: 1
    .uses_dynamic_stack: false
    .vgpr_count:     6
    .vgpr_spill_count: 0
    .wavefront_size: 64
  - .agpr_count:     8
    .args:
      - .actual_access:  read_only
        .address_space:  global
        .offset:         0
        .size:           8
        .value_kind:     global_buffer
      - .actual_access:  read_only
        .address_space:  global
        .offset:         8
        .size:           8
        .value_kind:     global_buffer
      - .actual_access:  read_only
        .address_space:  global
        .offset:         16
        .size:           8
        .value_kind:     global_buffer
      - .actual_access:  read_only
        .address_space:  global
        .offset:         24
        .size:           8
        .value_kind:     global_buffer
      - .actual_access:  read_only
        .address_space:  global
        .offset:         32
        .size:           8
        .value_kind:     global_buffer
      - .actual_access:  read_only
        .address_space:  global
        .offset:         40
        .size:           8
        .value_kind:     global_buffer
      - .actual_access:  write_only
        .address_space:  global
        .offset:         48
        .size:           8
        .value_kind:     global_buffer
      - .actual_access:  write_only
        .address_space:  global
        .offset:         56
        .size:           8
        .value_kind:     global_buffer
      - .actual_access:  write_only
        .address_space:  global
        .offset:         64
        .size:           8
        .value_kind:     global_buffer
    .group_segment_fixed_size: 10240
    .kernarg_segment_align: 8
    .kernarg_segment_size: 72
    .language:       OpenCL C
    .language_version:
      - 2
      - 0
    .max_flat_workgroup_size: 256
    .name:           _Z10gates_fastPKtS0_PKfS2_S2_S2_PtS3_S3_
    .private_segment_fixed_size: 0
    .sgpr_count:     24
    .sgpr_spill_count: 0
    .symbol:         _Z10gates_fastPKtS0_PKfS2_S2_S2_PtS3_S3_.kd
    .uniform_work_group_size: 1
    .uses_dynamic_stack: false
    .vgpr_count:     96
    .vgpr_spill_count: 0
    .wavefront_size: 64
  - .agpr_count:     4
    .args:
      - .actual_access:  read_only
        .address_space:  global
        .offset:         0
        .size:           8
        .value_kind:     global_buffer
      - .actual_access:  read_only
        .address_space:  global
        .offset:         8
        .size:           8
        .value_kind:     global_buffer
      - .actual_access:  read_only
        .address_space:  global
        .offset:         16
        .size:           8
        .value_kind:     global_buffer
      - .actual_access:  read_only
        .address_space:  global
        .offset:         24
        .size:           8
        .value_kind:     global_buffer
      - .actual_access:  write_only
        .address_space:  global
        .offset:         32
        .size:           8
        .value_kind:     global_buffer
      - .actual_access:  write_only
        .address_space:  global
        .offset:         40
        .size:           8
        .value_kind:     global_buffer
      - .actual_access:  write_only
        .address_space:  global
        .offset:         48
        .size:           8
        .value_kind:     global_buffer
    .group_segment_fixed_size: 0
    .kernarg_segment_align: 8
    .kernarg_segment_size: 56
    .language:       OpenCL C
    .language_version:
      - 2
      - 0
    .max_flat_workgroup_size: 256
    .name:           _Z10state_fastPKtS0_S0_S0_PtS1_Pf
    .private_segment_fixed_size: 0
    .sgpr_count:     20
    .sgpr_spill_count: 0
    .symbol:         _Z10state_fastPKtS0_S0_S0_PtS1_Pf.kd
    .uniform_work_group_size: 1
    .uses_dynamic_stack: false
    .vgpr_count:     184
    .vgpr_spill_count: 0
    .wavefront_size: 64
  - .agpr_count:     0
    .args:
      - .actual_access:  read_only
        .address_space:  global
        .offset:         0
        .size:           8
        .value_kind:     global_buffer
      - .actual_access:  read_only
        .address_space:  global
        .offset:         8
        .size:           8
        .value_kind:     global_buffer
      - .actual_access:  read_only
        .address_space:  global
        .offset:         16
        .size:           8
        .value_kind:     global_buffer
      - .actual_access:  write_only
        .address_space:  global
        .offset:         24
        .size:           8
        .value_kind:     global_buffer
      - .actual_access:  write_only
        .address_space:  global
        .offset:         32
        .size:           8
        .value_kind:     global_buffer
      - .actual_access:  write_only
        .address_space:  global
        .offset:         40
        .size:           8
        .value_kind:     global_buffer
    .group_segment_fixed_size: 0
    .kernarg_segment_align: 8
    .kernarg_segment_size: 48
    .language:       OpenCL C
    .language_version:
      - 2
      - 0
    .max_flat_workgroup_size: 256
    .name:           _Z11prefix_fastPKtS0_PKfPtS3_Pf
    .private_segment_fixed_size: 0
    .sgpr_count:     106
    .sgpr_spill_count: 41
    .symbol:         _Z11prefix_fastPKtS0_PKfPtS3_Pf.kd
    .uniform_work_group_size: 1
    .uses_dynamic_stack: false
    .vgpr_count:     205
    .vgpr_spill_count: 0
    .wavefront_size: 64
  - .agpr_count:     0
    .args:
      - .address_space:  global
        .offset:         0
        .size:           8
        .value_kind:     global_buffer
      - .address_space:  global
        .offset:         8
        .size:           8
        .value_kind:     global_buffer
      - .address_space:  global
        .offset:         16
        .size:           8
        .value_kind:     global_buffer
      - .actual_access:  read_only
        .address_space:  global
        .offset:         24
        .size:           8
        .value_kind:     global_buffer
      - .address_space:  global
        .offset:         32
        .size:           8
        .value_kind:     global_buffer
      - .address_space:  global
        .offset:         40
        .size:           8
        .value_kind:     global_buffer
      - .address_space:  global
        .offset:         48
        .size:           8
        .value_kind:     global_buffer
      - .address_space:  global
        .offset:         56
        .size:           8
        .value_kind:     global_buffer
      - .address_space:  global
        .offset:         64
        .size:           8
        .value_kind:     global_buffer
      - .address_space:  global
        .offset:         72
        .size:           8
        .value_kind:     global_buffer
      - .address_space:  global
        .offset:         80
        .size:           8
        .value_kind:     global_buffer
      - .actual_access:  write_only
        .address_space:  global
        .offset:         88
        .size:           8
        .value_kind:     global_buffer
    .group_segment_fixed_size: 0
    .kernarg_segment_align: 8
    .kernarg_segment_size: 96
    .language:       OpenCL C
    .language_version:
      - 2
      - 0
    .max_flat_workgroup_size: 512
    .name:           _Z9attn_fastPKtS0_S0_S0_S0_S0_S0_S0_S0_PKfS2_Pt
    .private_segment_fixed_size: 0
    .sgpr_count:     54
    .sgpr_spill_count: 0
    .symbol:         _Z9attn_fastPKtS0_S0_S0_S0_S0_S0_S0_S0_PKfS2_Pt.kd
    .uniform_work_group_size: 1
    .uses_dynamic_stack: false
    .vgpr_count:     224
    .vgpr_spill_count: 0
    .wavefront_size: 64
  - .agpr_count:     12
    .args:
      - .actual_access:  read_only
        .address_space:  global
        .offset:         0
        .size:           8
        .value_kind:     global_buffer
      - .actual_access:  read_only
        .address_space:  global
        .offset:         8
        .size:           8
        .value_kind:     global_buffer
      - .actual_access:  read_only
        .address_space:  global
        .offset:         16
        .size:           8
        .value_kind:     global_buffer
      - .actual_access:  read_only
        .address_space:  global
        .offset:         24
        .size:           8
        .value_kind:     global_buffer
      - .actual_access:  read_only
        .address_space:  global
        .offset:         32
        .size:           8
        .value_kind:     global_buffer
      - .actual_access:  read_only
        .address_space:  global
        .offset:         40
        .size:           8
        .value_kind:     global_buffer
      - .actual_access:  read_only
        .address_space:  global
        .offset:         48
        .size:           8
        .value_kind:     global_buffer
      - .actual_access:  read_only
        .address_space:  global
        .offset:         56
        .size:           8
        .value_kind:     global_buffer
      - .actual_access:  read_only
        .address_space:  global
        .offset:         64
        .size:           8
        .value_kind:     global_buffer
      - .actual_access:  read_only
        .address_space:  global
        .offset:         72
        .size:           8
        .value_kind:     global_buffer
      - .actual_access:  read_only
        .address_space:  global
        .offset:         80
        .size:           8
        .value_kind:     global_buffer
      - .actual_access:  read_only
        .address_space:  global
        .offset:         88
        .size:           8
        .value_kind:     global_buffer
      - .actual_access:  write_only
        .address_space:  global
        .offset:         96
        .size:           8
        .value_kind:     global_buffer
      - .actual_access:  write_only
        .address_space:  global
        .offset:         104
        .size:           8
        .value_kind:     global_buffer
      - .actual_access:  write_only
        .address_space:  global
        .offset:         112
        .size:           8
        .value_kind:     global_buffer
      - .actual_access:  write_only
        .address_space:  global
        .offset:         120
        .size:           8
        .value_kind:     global_buffer
      - .actual_access:  write_only
        .address_space:  global
        .offset:         128
        .size:           8
        .value_kind:     global_buffer
      - .actual_access:  write_only
        .address_space:  global
        .offset:         136
        .size:           8
        .value_kind:     global_buffer
    .group_segment_fixed_size: 16640
    .kernarg_segment_align: 8
    .kernarg_segment_size: 144
    .language:       OpenCL C
    .language_version:
      - 2
      - 0
    .max_flat_workgroup_size: 256
    .name:           _Z11prep_kernelPKfS0_S0_S0_S0_S0_S0_S0_S0_S0_S0_S0_PtS1_S1_S1_S1_S1_
    .private_segment_fixed_size: 0
    .sgpr_count:     46
    .sgpr_spill_count: 0
    .symbol:         _Z11prep_kernelPKfS0_S0_S0_S0_S0_S0_S0_S0_S0_S0_S0_PtS1_S1_S1_S1_S1_.kd
    .uniform_work_group_size: 1
    .uses_dynamic_stack: false
    .vgpr_count:     168
    .vgpr_spill_count: 0
    .wavefront_size: 64
  - .agpr_count:     0
    .args:
      - .address_space:  global
        .offset:         0
        .size:           8
        .value_kind:     global_buffer
      - .address_space:  global
        .offset:         8
        .size:           8
        .value_kind:     global_buffer
      - .offset:         16
        .size:           4
        .value_kind:     by_value
      - .offset:         20
        .size:           4
        .value_kind:     by_value
      - .offset:         24
        .size:           4
        .value_kind:     by_value
      - .offset:         28
        .size:           4
        .value_kind:     by_value
      - .address_space:  global
        .offset:         32
        .size:           8
        .value_kind:     global_buffer
    .group_segment_fixed_size: 0
    .kernarg_segment_align: 8
    .kernarg_segment_size: 40
    .language:       OpenCL C
    .language_version:
      - 2
      - 0
    .max_flat_workgroup_size: 1024
    .name:           _Z9dbg_cmp16PKtS0_iiffPf
    .private_segment_fixed_size: 0
    .sgpr_count:     18
    .sgpr_spill_count: 0
    .symbol:         _Z9dbg_cmp16PKtS0_iiffPf.kd
    .uniform_work_group_size: 1
    .uses_dynamic_stack: false
    .vgpr_count:     5
    .vgpr_spill_count: 0
    .wavefront_size: 64
  - .agpr_count:     0
    .args:
      - .address_space:  global
        .offset:         0
        .size:           8
        .value_kind:     global_buffer
      - .address_space:  global
        .offset:         8
        .size:           8
        .value_kind:     global_buffer
      - .offset:         16
        .size:           4
        .value_kind:     by_value
      - .offset:         20
        .size:           4
        .value_kind:     by_value
      - .offset:         24
        .size:           56
        .value_kind:     by_value
    .group_segment_fixed_size: 0
    .kernarg_segment_align: 8
    .kernarg_segment_size: 80
    .language:       OpenCL C
    .language_version:
      - 2
      - 0
    .max_flat_workgroup_size: 512
    .name:           _Z5gemm8ILi0EEvPKtS1_ii7EpiArgs
    .private_segment_fixed_size: 0
    .sgpr_count:     36
    .sgpr_spill_count: 0
    .symbol:         _Z5gemm8ILi0EEvPKtS1_ii7EpiArgs.kd
    .uniform_work_group_size: 1
    .uses_dynamic_stack: false
    .vgpr_count:     246
    .vgpr_spill_count: 0
    .wavefront_size: 64
  - .agpr_count:     0
    .args:
      - .address_space:  global
        .offset:         0
        .size:           8
        .value_kind:     global_buffer
      - .address_space:  global
        .offset:         8
        .size:           8
        .value_kind:     global_buffer
      - .address_space:  global
        .offset:         16
        .size:           8
        .value_kind:     global_buffer
      - .address_space:  global
        .offset:         24
        .size:           8
        .value_kind:     global_buffer
      - .actual_access:  write_only
        .address_space:  global
        .offset:         32
        .size:           8
        .value_kind:     global_buffer
      - .actual_access:  write_only
        .address_space:  global
        .offset:         40
        .size:           8
        .value_kind:     global_buffer
      - .actual_access:  write_only
        .address_space:  global
        .offset:         48
        .size:           8
        .value_kind:     global_buffer
    .group_segment_fixed_size: 81920
    .kernarg_segment_align: 8
    .kernarg_segment_size: 56
    .language:       OpenCL C
    .language_version:
      - 2
      - 0
    .max_flat_workgroup_size: 256
    .name:           _Z9scan_fastILb1EEvPKtS1_S1_S1_PtS2_Pf
    .private_segment_fixed_size: 0
    .sgpr_count:     62
    .sgpr_spill_count: 0
    .symbol:         _Z9scan_fastILb1EEvPKtS1_S1_S1_PtS2_Pf.kd
    .uniform_work_group_size: 1
    .uses_dynamic_stack: false
    .vgpr_count:     160
    .vgpr_spill_count: 0
    .wavefront_size: 64
